# v7 + early L2 warm-up at kernel start + sc1 on centers/outq stores
# baseline (speedup 1.0000x reference)
_Z7k3_mainPKhPKfS2_S2_S2_PfS3_S3_:
	s_load_dwordx4 s[40:43], s[0:1], 0x0
	s_load_dwordx2 s[48:49], s[0:1], 0x10
	s_lshl_b32 s3, s2, 5
	s_and_b32 s3, s3, 0xe0
	s_lshr_b32 s2, s2, 3
	v_and_b32_e32 v128, 63, v0
	s_add_i32 s4, s3, s2
	s_waitcnt lgkmcnt(0)
	s_add_u32 s2, s40, 0x784000
	v_or_b32_e32 v134, 64, v128
	s_addc_u32 s3, s41, 0
	v_lshlrev_b32_e32 v98, 4, v128
	v_lshlrev_b32_e32 v1, 4, v134
	v_or_b32_e32 v133, 0x80, v128
	global_load_dwordx4 v[2:5], v98, s[2:3]
	global_load_dwordx4 v[6:9], v1, s[2:3]
	v_lshlrev_b32_e32 v1, 4, v133
	global_load_dwordx4 v[10:13], v1, s[2:3]
	v_or_b32_e32 v1, 0xc00, v98
	global_load_dwordx4 v[42:45], v1, s[2:3]
	s_load_dwordx2 s[2:3], s[0:1], 0x20
	v_lshrrev_b32_e32 v150, 6, v0
	s_lshl_b32 s33, s4, 4
	v_or_b32_e32 v66, s33, v150
	v_ashrrev_i32_e32 v67, 31, v66
	v_lshlrev_b64 v[14:15], 12, v[66:67]
	v_mov_b32_e32 v99, 0
	s_waitcnt lgkmcnt(0)
	v_lshl_add_u64 v[14:15], s[2:3], 0, v[14:15]
	v_lshl_add_u64 v[14:15], v[14:15], 0, v[98:99]
	global_load_dwordx4 v[54:57], v[14:15], off
	global_load_dwordx4 v[58:61], v[14:15], off offset:1024
	global_load_dwordx4 v[62:65], v[14:15], off offset:2048
	s_lshr_b32 s59, s33, 4
	s_and_b32 s59, s59, 31
	s_lshl_b32 s59, s59, 15
	s_add_u32 s59, s59, 0x787000
	s_add_u32 s68, s40, s59
	s_addc_u32 s69, s41, 0
	v_lshlrev_b32_e32 v207, 6, v0
	global_load_dword v207, v207, s[68:69]
	s_movk_i32 s4, 0xc00
	v_mov_b64_e32 v[16:17], s[42:43]
	v_mad_i64_i32 v[18:19], s[6:7], v66, s4, v[16:17]
	v_lshl_add_u64 v[18:19], v[18:19], 0, v[98:99]
	global_load_dwordx4 v[38:41], v[18:19], off
	global_load_dwordx4 v[34:37], v[18:19], off offset:1024
	global_load_dwordx4 v[30:33], v[18:19], off offset:2048
	global_load_dwordx4 v[68:71], v[14:15], off offset:3072
	v_mov_b32_e32 v50, v99
	v_mov_b32_e32 v51, v99
	v_mov_b32_e32 v52, v99
	v_mbcnt_lo_u32_b32 v1, -1, 0
	v_mov_b32_e32 v53, v99
	v_mbcnt_hi_u32_b32 v129, -1, v1
	v_and_b32_e32 v132, 64, v129
	v_xor_b32_e32 v1, 16, v129
	v_add_u32_e32 v130, 64, v132
	s_mov_b32 s5, 0xff61b1e6
	v_cmp_lt_i32_e32 vcc, v1, v130
	v_lshlrev_b32_e32 v135, 2, v128
	v_or_b32_e32 v146, 1, v135
	v_cndmask_b32_e32 v1, v129, v1, vcc
	v_or_b32_e32 v148, 2, v135
	v_or_b32_e32 v149, 3, v135
	v_or_b32_e32 v147, 0x100, v135
	v_or_b32_e32 v152, 0x101, v135
	v_or_b32_e32 v153, 0x102, v135
	v_or_b32_e32 v137, 0x103, v135
	v_or_b32_e32 v136, 0x200, v135
	v_or_b32_e32 v138, 0x201, v135
	v_or_b32_e32 v140, 0x202, v135
	v_or_b32_e32 v141, 0x203, v135
	v_or_b32_e32 v139, 0x300, v135
	v_or_b32_e32 v143, 0x301, v135
	v_or_b32_e32 v144, 0x302, v135
	s_add_u32 s50, s40, 0x780000
	s_addc_u32 s51, s41, 0
	v_or_b32_e32 v145, 0x303, v135
	v_lshl_add_u64 v[22:23], v[66:67], 2, s[50:51]
	global_load_dword v67, v[22:23], off
	v_lshlrev_b32_e32 v1, 2, v1
	v_or_b32_e32 v20, 8, v66
	v_ashrrev_i32_e32 v21, 31, v20
	v_mad_i64_i32 v[16:17], s[6:7], v20, s4, v[16:17]
	v_lshlrev_b64 v[18:19], 12, v[20:21]
	v_lshl_add_u64 v[46:47], v[16:17], 0, v[98:99]
	v_lshl_add_u64 v[16:17], s[2:3], 0, v[18:19]
	v_lshl_add_u64 v[48:49], v[16:17], 0, v[98:99]
	global_load_dwordx4 v[26:29], v[48:49], off
	global_load_dwordx4 v[22:25], v[48:49], off offset:1024
	global_load_dwordx4 v[18:21], v[48:49], off offset:2048
	global_load_dwordx4 v[14:17], v[48:49], off offset:3072
	s_waitcnt vmcnt(15)
	v_max_f32_e32 v5, v5, v5
	v_max_f32_e32 v4, v4, v4
	s_waitcnt vmcnt(14)
	v_max_f32_e32 v9, v9, v9
	v_max_f32_e32 v8, v8, v8
	s_waitcnt vmcnt(13)
	v_max_f32_e32 v13, v13, v13
	v_max_f32_e32 v12, v12, v12
	s_waitcnt vmcnt(12)
	v_max_f32_e32 v45, v45, v45
	v_max_f32_e32 v44, v44, v44
	v_max_f32_e32 v4, v4, v5
	v_max_f32_e32 v5, v8, v9
	v_max_f32_e32 v8, v12, v13
	v_max_f32_e32 v9, v44, v45
	v_max3_f32 v2, v2, v3, v4
	v_max3_f32 v3, v6, v7, v5
	v_max3_f32 v4, v10, v11, v8
	v_max3_f32 v5, v42, v43, v9
	v_max3_f32 v2, v2, 0, v3
	v_max3_f32 v2, v2, v4, v5
	s_waitcnt vmcnt(11)
	v_cmp_lt_f32_e32 vcc, s5, v54
	v_mov_b32_dpp v50, v2 row_ror:1 row_mask:0xf bank_mask:0xf
	v_max_f32_e32 v4, v50, v50
	v_max_f32_e32 v2, v2, v4
	v_cndmask_b32_e32 v3, 0, v135, vcc
	s_nop 0
	v_mov_b32_dpp v51, v2 row_ror:2 row_mask:0xf bank_mask:0xf
	v_max_f32_e32 v4, v51, v51
	v_max_f32_e32 v2, v2, v4
	s_nop 1
	v_mov_b32_dpp v52, v2 row_ror:4 row_mask:0xf bank_mask:0xf
	v_max_f32_e32 v4, v52, v52
	v_max_f32_e32 v2, v2, v4
	s_nop 1
	v_mov_b32_dpp v53, v2 row_ror:8 row_mask:0xf bank_mask:0xf
	v_max_f32_e32 v4, v53, v53
	v_max_f32_e32 v42, v2, v4
	v_max_f32_e32 v2, v54, v54
	v_max_f32_e32 v2, 0xff61b1e6, v2
	v_cmp_gt_f32_e32 vcc, v55, v2
	v_xor_b32_e32 v4, 32, v129
	ds_bpermute_b32 v43, v1, v42
	v_cndmask_b32_e32 v2, v2, v55, vcc
	v_cndmask_b32_e32 v3, v3, v146, vcc
	v_cmp_gt_f32_e32 vcc, v56, v2
	s_waitcnt lgkmcnt(0)
	v_max_f32_e32 v43, v43, v43
	v_cndmask_b32_e32 v2, v2, v56, vcc
	v_cndmask_b32_e32 v3, v3, v148, vcc
	v_cmp_gt_f32_e32 vcc, v57, v2
	v_max_f32_e32 v75, v42, v43
	v_mov_b64_e32 v[42:43], s[48:49]
	v_cndmask_b32_e32 v2, v2, v57, vcc
	v_cndmask_b32_e32 v3, v3, v149, vcc
	s_waitcnt vmcnt(10)
	v_cmp_gt_f32_e32 vcc, v58, v2
	s_nop 1
	v_cndmask_b32_e32 v2, v2, v58, vcc
	v_cndmask_b32_e32 v3, v3, v147, vcc
	v_cmp_gt_f32_e32 vcc, v59, v2
	s_nop 1
	v_cndmask_b32_e32 v2, v2, v59, vcc
	v_cndmask_b32_e32 v3, v3, v152, vcc
	v_cmp_gt_f32_e32 vcc, v60, v2
	s_nop 1
	v_cndmask_b32_e32 v2, v2, v60, vcc
	v_cndmask_b32_e32 v3, v3, v153, vcc
	v_cmp_gt_f32_e32 vcc, v61, v2
	s_nop 1
	v_cndmask_b32_e32 v2, v2, v61, vcc
	v_cndmask_b32_e32 v3, v3, v137, vcc
	s_waitcnt vmcnt(9)
	v_cmp_gt_f32_e32 vcc, v62, v2
	s_nop 1
	v_cndmask_b32_e32 v2, v2, v62, vcc
	v_cndmask_b32_e32 v3, v3, v136, vcc
	v_cmp_gt_f32_e32 vcc, v63, v2
	s_nop 1
	v_cndmask_b32_e32 v2, v2, v63, vcc
	v_cndmask_b32_e32 v3, v3, v138, vcc
	v_cmp_gt_f32_e32 vcc, v64, v2
	s_nop 1
	v_cndmask_b32_e32 v2, v2, v64, vcc
	v_cndmask_b32_e32 v3, v3, v140, vcc
	v_cmp_gt_f32_e32 vcc, v65, v2
	s_nop 1
	v_cndmask_b32_e32 v2, v2, v65, vcc
	v_cndmask_b32_e32 v3, v3, v141, vcc
	s_waitcnt vmcnt(5)
	v_cmp_gt_f32_e32 vcc, v68, v2
	s_nop 1
	v_cndmask_b32_e32 v2, v2, v68, vcc
	v_cndmask_b32_e32 v3, v3, v139, vcc
	v_cmp_gt_f32_e32 vcc, v69, v2
	s_nop 1
	v_cndmask_b32_e32 v2, v2, v69, vcc
	v_cndmask_b32_e32 v3, v3, v143, vcc
	v_cmp_gt_f32_e32 vcc, v70, v2
	s_nop 1
	v_cndmask_b32_e32 v2, v2, v70, vcc
	v_cndmask_b32_e32 v3, v3, v144, vcc
	v_cmp_gt_f32_e32 vcc, v71, v2
	s_nop 1
	v_cndmask_b32_e32 v45, v2, v71, vcc
	v_mov_b32_e32 v2, v99
	v_cndmask_b32_e32 v44, v3, v145, vcc
	v_max_f32_e32 v3, v45, v45
	v_mov_b32_dpp v2, v45 row_ror:1 row_mask:0xf bank_mask:0xf
	v_max_f32_e32 v2, v2, v2
	v_max_f32_e32 v2, v3, v2
	v_mov_b32_e32 v3, v99
	v_cmp_lt_i32_e32 vcc, v4, v130
	s_nop 0
	v_mov_b32_dpp v3, v2 row_ror:2 row_mask:0xf bank_mask:0xf
	v_max_f32_e32 v3, v3, v3
	v_max_f32_e32 v2, v2, v3
	v_mov_b32_e32 v3, v99
	v_cndmask_b32_e32 v4, v129, v4, vcc
	v_lshlrev_b32_e32 v151, 2, v4
	v_mov_b32_dpp v3, v2 row_ror:4 row_mask:0xf bank_mask:0xf
	v_max_f32_e32 v3, v3, v3
	v_max_f32_e32 v2, v2, v3
	v_mov_b32_e32 v3, v99
	ds_bpermute_b32 v76, v151, v75
	s_nop 0
	v_mov_b32_dpp v3, v2 row_ror:8 row_mask:0xf bank_mask:0xf
	v_max_f32_e32 v3, v3, v3
	v_max_f32_e32 v2, v2, v3
	ds_bpermute_b32 v3, v1, v2
	s_waitcnt lgkmcnt(0)
	v_max_f32_e32 v3, v3, v3
	v_max_f32_e32 v48, v2, v3
	ds_bpermute_b32 v49, v151, v48
	global_load_dwordx4 v[10:13], v[46:47], off
	global_load_dwordx4 v[6:9], v[46:47], off offset:1024
	global_load_dwordx4 v[2:5], v[46:47], off offset:2048
	s_waitcnt lgkmcnt(0)
	v_max_f32_e32 v46, v49, v49
	v_max_f32_e32 v74, v48, v46
	v_cmp_eq_f32_e32 vcc, v45, v74
	s_ff1_i32_b64 s2, vcc
	s_cmp_lg_u64 vcc, 0
	s_cselect_b32 s2, s2, 63
	v_or_b32_e32 v45, s2, v132
	v_lshlrev_b32_e32 v45, 2, v45
	ds_bpermute_b32 v44, v45, v44
	s_waitcnt lgkmcnt(0)
	v_mad_i64_i32 v[42:43], s[2:3], v44, s4, v[42:43]
	v_lshl_add_u64 v[72:73], v[42:43], 0, v[98:99]
	global_load_dwordx4 v[42:45], v[72:73], off
	global_load_dwordx4 v[46:49], v[72:73], off offset:1024
	global_load_dwordx4 v[50:53], v[72:73], off offset:2048
	v_max_f32_e32 v72, v76, v76
	v_max_f32_e32 v142, v75, v72
	s_waitcnt vmcnt(10)
	v_mul_f32_e32 v67, v142, v67
	s_mov_b32 s2, 0xf800000
	v_mul_f32_e32 v72, 0x4f800000, v67
	v_cmp_gt_f32_e32 vcc, s2, v67
	v_mad_i64_i32 v[90:91], s[2:3], v66, s4, 0
	s_nop 0
	v_cndmask_b32_e32 v67, v67, v72, vcc
	v_sqrt_f32_e32 v72, v67
	v_mov_b32_e32 v66, 0x1c000
	v_cmp_eq_u32_e64 s[2:3], 0, v128
	v_lshl_or_b32 v131, v150, 8, v66
	v_add_u32_e32 v73, -1, v72
	v_fma_f32 v75, -v73, v72, v67
	v_cmp_ge_f32_e64 s[4:5], 0, v75
	v_add_u32_e32 v75, 1, v72
	s_nop 0
	v_cndmask_b32_e64 v73, v72, v73, s[4:5]
	v_fma_f32 v72, -v75, v72, v67
	v_cmp_lt_f32_e64 s[4:5], 0, v72
	s_nop 1
	v_cndmask_b32_e64 v72, v73, v75, s[4:5]
	v_mul_f32_e32 v73, 0x37800000, v72
	v_cndmask_b32_e32 v72, v72, v73, vcc
	v_mov_b32_e32 v73, 0x260
	v_cmp_class_f32_e32 vcc, v67, v73
	s_nop 1
	v_cndmask_b32_e32 v67, v72, v67, vcc
	v_fmamk_f32 v67, v67, 0xbbb8cfc0, v74
	v_cmp_ge_f32_e64 s[36:37], v54, v67
	v_cmp_ge_f32_e64 s[34:35], v55, v67
	s_bcnt1_i32_b64 s4, s[36:37]
	s_bcnt1_i32_b64 s5, s[34:35]
	v_cmp_ge_f32_e64 s[30:31], v56, v67
	s_add_i32 s4, s4, s5
	s_bcnt1_i32_b64 s5, s[30:31]
	v_cmp_ge_f32_e64 s[28:29], v57, v67
	s_add_i32 s4, s4, s5
	s_bcnt1_i32_b64 s5, s[28:29]
	v_cmp_ge_f32_e64 s[26:27], v58, v67
	s_add_i32 s4, s4, s5
	s_bcnt1_i32_b64 s5, s[26:27]
	v_cmp_ge_f32_e64 s[24:25], v59, v67
	s_add_i32 s4, s4, s5
	s_bcnt1_i32_b64 s5, s[24:25]
	v_cmp_ge_f32_e64 s[22:23], v60, v67
	s_add_i32 s4, s4, s5
	s_bcnt1_i32_b64 s5, s[22:23]
	v_cmp_ge_f32_e64 s[20:21], v61, v67
	s_add_i32 s4, s4, s5
	s_bcnt1_i32_b64 s5, s[20:21]
	v_cmp_ge_f32_e64 s[18:19], v62, v67
	s_add_i32 s4, s4, s5
	s_bcnt1_i32_b64 s5, s[18:19]
	v_cmp_ge_f32_e64 s[16:17], v63, v67
	s_add_i32 s4, s4, s5
	s_bcnt1_i32_b64 s5, s[16:17]
	v_cmp_ge_f32_e64 s[14:15], v64, v67
	s_add_i32 s4, s4, s5
	s_bcnt1_i32_b64 s5, s[14:15]
	v_cmp_ge_f32_e64 s[12:13], v65, v67
	s_add_i32 s4, s4, s5
	s_bcnt1_i32_b64 s5, s[12:13]
	v_cmp_ge_f32_e64 s[10:11], v68, v67
	s_add_i32 s4, s4, s5
	s_bcnt1_i32_b64 s5, s[10:11]
	v_cmp_ge_f32_e64 s[8:9], v69, v67
	s_add_i32 s4, s4, s5
	s_bcnt1_i32_b64 s5, s[8:9]
	v_cmp_ge_f32_e64 s[6:7], v70, v67
	s_add_i32 s4, s4, s5
	s_bcnt1_i32_b64 s5, s[6:7]
	s_add_i32 s38, s4, s5
	v_cmp_ge_f32_e64 s[4:5], v71, v67
	s_bcnt1_i32_b64 s39, s[4:5]
	s_add_i32 s38, s38, s39
	s_cmpk_lt_u32 s38, 0x41
	s_cbranch_scc0 .LBB2_7
	s_cmp_gt_u32 s38, 1
	s_waitcnt vmcnt(0)
	v_mov_b64_e32 v[56:57], v[52:53]
	v_mov_b64_e32 v[54:55], v[50:51]
	v_mov_b64_e32 v[60:61], v[48:49]
	v_mov_b64_e32 v[58:59], v[46:47]
	v_mov_b64_e32 v[64:65], v[44:45]
	v_mov_b64_e32 v[62:63], v[42:43]
	s_cbranch_scc0 .LBB2_94
	v_cndmask_b32_e64 v54, 0, 1, s[36:37]
	s_mov_b32 s42, 0
	v_cmp_ne_u32_e32 vcc, 0, v54
	s_cbranch_vccz .LBB2_8
	v_mov_b32_e32 v54, 0x1c000
	v_lshl_or_b32 v54, v150, 8, v54
	s_branch .LBB2_5

.LBB2_207:
	s_waitcnt vmcnt(2)
	v_mul_u32_u24_e32 v44, 0xc00, v150
	v_or_b32_e32 v44, v44, v98
	v_or_b32_e32 v45, 0x10000, v44
	s_mov_b32 s5, 0x2aaaaaab
	s_load_dwordx2 s[38:39], s[0:1], 0x18
	s_load_dwordx4 s[44:47], s[0:1], 0x30
	ds_write_b128 v45, v[62:65]
	v_mul_hi_u32 v45, v135, s5
	s_waitcnt vmcnt(1)
	v_mul_i32_i24_e32 v46, -6, v45
	v_and_b32_e32 v47, 2, v46
	v_lshlrev_b32_e32 v101, 5, v45
	v_add_lshl_u32 v46, v46, v135, 2
	v_and_b32_e32 v102, 0xffffff0, v46
	v_or_b32_e32 v46, v101, v150
	v_add_u32_e32 v48, v46, v102
	v_lshlrev_b32_e32 v103, 2, v47
	v_sub_f32_e32 v38, v38, v62
	v_lshl_or_b32 v47, v48, 4, v103
	ds_write_b32 v47, v38
	v_mad_i32_i24 v38, v45, -6, v146
	v_and_b32_e32 v45, 3, v38
	v_lshlrev_b32_e32 v38, 2, v38
	v_and_b32_e32 v104, 0xffffff0, v38
	v_add_u32_e32 v38, v46, v104
	v_lshlrev_b32_e32 v105, 2, v45
	v_sub_f32_e32 v39, v39, v63
	v_lshl_or_b32 v38, v38, 4, v105
	ds_write_b32 v38, v39
	v_mul_hi_u32 v38, v148, s5
	v_mad_i32_i24 v39, v38, -6, v148
	v_lshlrev_b32_e32 v106, 5, v38
	v_lshlrev_b32_e32 v38, 2, v39
	v_and_b32_e32 v45, 2, v39
	v_and_b32_e32 v107, 0xffffff0, v38
	v_or_b32_e32 v38, v106, v150
	v_add_u32_e32 v38, v38, v107
	v_lshlrev_b32_e32 v108, 2, v45
	v_sub_f32_e32 v40, v40, v64
	v_lshl_or_b32 v38, v38, 4, v108
	ds_write_b32 v38, v40
	v_mul_hi_u32 v38, v149, s5
	v_mad_i32_i24 v39, v38, -6, v149
	v_lshlrev_b32_e32 v109, 5, v38
	v_lshlrev_b32_e32 v38, 2, v39
	v_and_b32_e32 v40, 3, v39
	v_and_b32_e32 v110, 0xffffff0, v38
	v_or_b32_e32 v38, v109, v150
	v_add_u32_e32 v38, v38, v110
	v_lshlrev_b32_e32 v111, 2, v40
	v_sub_f32_e32 v41, v41, v65
	v_lshl_or_b32 v38, v38, 4, v111
	ds_write_b32 v38, v41
	v_add_u32_e32 v38, 0x10400, v44
	ds_write_b128 v38, v[58:61]
	v_sub_f32_e32 v38, v34, v58
	v_sub_f32_e32 v39, v35, v59
	v_pk_add_f32 v[34:35], v[36:37], v[60:61] neg_lo:[0,1] neg_hi:[0,1]
	v_lshlrev_b32_e32 v36, 2, v134
	v_mul_hi_u32 v37, v36, s5
	v_mad_i32_i24 v41, v37, -6, v36
	v_mul_i32_i24_e32 v40, -6, v37
	v_lshlrev_b32_e32 v112, 5, v37
	v_lshlrev_b32_e32 v37, 2, v41
	v_and_b32_e32 v40, 2, v40
	v_and_b32_e32 v113, 0xffffff0, v37
	v_or_b32_e32 v37, v112, v150
	v_add_u32_e32 v45, v37, v113
	v_lshlrev_b32_e32 v114, 2, v40
	v_lshl_or_b32 v40, v45, 4, v114
	ds_write_b32 v40, v38
	v_or_b32_e32 v38, 1, v41
	v_lshlrev_b32_e32 v38, 2, v38
	v_bitop3_b32 v40, v41, 3, 1 bitop3:0xc8
	v_and_b32_e32 v115, 0xffffff0, v38
	v_add_u32_e32 v37, v37, v115
	v_lshlrev_b32_e32 v116, 2, v40
	v_lshl_or_b32 v37, v37, 4, v116
	ds_write_b32 v37, v39
	v_or_b32_e32 v37, 2, v36
	v_mul_hi_u32 v38, v37, s5
	v_mad_i32_i24 v37, v38, -6, v37
	v_and_b32_e32 v39, 2, v37
	v_lshlrev_b32_e32 v117, 5, v38
	v_lshlrev_b32_e32 v37, 2, v37
	v_and_b32_e32 v118, 0xffffff0, v37
	v_or_b32_e32 v37, v117, v150
	v_add_u32_e32 v37, v37, v118
	v_lshlrev_b32_e32 v119, 2, v39
	v_lshl_or_b32 v37, v37, 4, v119
	ds_write_b32 v37, v34
	v_or_b32_e32 v34, 3, v36
	v_mul_hi_u32 v36, v34, s5
	v_mad_i32_i24 v34, v36, -6, v34
	s_waitcnt lgkmcnt(0)
	v_lshl_add_u64 v[42:43], s[42:43], 0, v[90:91]
	v_mov_b32_e32 v99, 0
	v_and_b32_e32 v37, 3, v34
	v_lshlrev_b32_e32 v120, 5, v36
	v_lshlrev_b32_e32 v34, 2, v34
	v_lshl_add_u64 v[42:43], v[42:43], 0, v[98:99]
	v_and_b32_e32 v121, 0xffffff0, v34
	v_or_b32_e32 v34, v120, v150
	global_store_dwordx4 v[42:43], v[62:65], off sc1
	global_store_dwordx4 v[42:43], v[58:61], off offset:1024 sc1
	v_add_u32_e32 v34, v34, v121
	v_lshlrev_b32_e32 v122, 2, v37
	global_store_dwordx4 v[42:43], v[54:57], off offset:2048 sc1
	v_pk_add_f32 v[42:43], v[32:33], v[56:57] neg_lo:[0,1] neg_hi:[0,1]
	v_lshlrev_b32_e32 v32, 2, v133
	v_lshl_or_b32 v34, v34, 4, v122
	v_mul_hi_u32 v33, v32, s5
	ds_write_b32 v34, v35
	v_add_u32_e32 v34, 0x10800, v44
	v_mad_i32_i24 v35, v33, -6, v32
	ds_write_b128 v34, v[54:57]
	v_mul_i32_i24_e32 v34, -6, v33
	v_lshlrev_b32_e32 v123, 5, v33
	v_lshlrev_b32_e32 v33, 2, v35
	v_and_b32_e32 v34, 2, v34
	v_and_b32_e32 v124, 0xffffff0, v33
	v_or_b32_e32 v33, v123, v150
	v_add_u32_e32 v36, v33, v124
	v_lshlrev_b32_e32 v125, 2, v34
	v_pk_add_f32 v[30:31], v[30:31], v[54:55] neg_lo:[0,1] neg_hi:[0,1]
	v_lshl_or_b32 v34, v36, 4, v125
	ds_write_b32 v34, v30
	v_or_b32_e32 v30, 1, v35
	v_lshlrev_b32_e32 v30, 2, v30
	v_bitop3_b32 v34, v35, 3, 1 bitop3:0xc8
	v_and_b32_e32 v126, 0xffffff0, v30
	v_add_u32_e32 v30, v33, v126
	v_lshlrev_b32_e32 v127, 2, v34
	v_lshl_or_b32 v30, v30, 4, v127
	ds_write_b32 v30, v31
	v_or_b32_e32 v30, 2, v32
	v_mul_hi_u32 v31, v30, s5
	v_mad_i32_i24 v30, v31, -6, v30
	v_and_b32_e32 v33, 2, v30
	v_lshlrev_b32_e32 v133, 5, v31
	v_lshlrev_b32_e32 v30, 2, v30
	s_mov_b32 s6, 0xff61b1e6
	v_max_f32_e32 v31, v26, v26
	v_and_b32_e32 v134, 0xffffff0, v30
	v_or_b32_e32 v30, v133, v150
	v_cmp_lt_f32_e32 vcc, s6, v26
	v_max_f32_e32 v31, 0xff61b1e6, v31
	v_add_u32_e32 v34, v30, v134
	v_cndmask_b32_e32 v30, 0, v135, vcc
	v_cmp_gt_f32_e32 vcc, v27, v31
	v_or_b32_e32 v154, 8, v150
	v_add_u32_e32 v62, s33, v154
	v_cndmask_b32_e32 v31, v31, v27, vcc
	v_cndmask_b32_e32 v30, v30, v146, vcc
	v_cmp_gt_f32_e32 vcc, v28, v31
	v_ashrrev_i32_e32 v63, 31, v62
	v_or_b32_e32 v32, 3, v32
	v_cndmask_b32_e32 v31, v31, v28, vcc
	v_cndmask_b32_e32 v30, v30, v148, vcc
	v_cmp_gt_f32_e32 vcc, v29, v31
	s_movk_i32 s4, 0xc00
	v_lshl_or_b32 v100, v128, 5, 16
	v_cndmask_b32_e32 v31, v31, v29, vcc
	v_cndmask_b32_e32 v30, v30, v149, vcc
	v_cmp_gt_f32_e32 vcc, v22, v31
	s_mov_b64 s[0:1], 0x3f800000
	s_nop 0
	v_cndmask_b32_e32 v31, v31, v22, vcc
	v_cndmask_b32_e32 v30, v30, v147, vcc
	v_cmp_gt_f32_e32 vcc, v23, v31
	s_nop 1
	v_cndmask_b32_e32 v31, v31, v23, vcc
	v_cndmask_b32_e32 v30, v30, v152, vcc
	v_cmp_gt_f32_e32 vcc, v24, v31
	s_nop 1
	v_cndmask_b32_e32 v35, v30, v153, vcc
	v_cndmask_b32_e32 v30, v31, v24, vcc
	v_cmp_gt_f32_e32 vcc, v25, v30
	s_nop 1
	v_cndmask_b32_e32 v36, v30, v25, vcc
	v_lshl_add_u64 v[30:31], v[62:63], 2, s[50:51]
	global_load_dword v46, v[30:31], off
	v_cndmask_b32_e32 v30, v35, v137, vcc
	v_cmp_gt_f32_e32 vcc, v18, v36
	v_mov_b32_e32 v35, v99
	v_lshlrev_b32_e32 v63, 2, v33
	v_cndmask_b32_e32 v31, v36, v18, vcc
	v_cndmask_b32_e32 v30, v30, v136, vcc
	v_cmp_gt_f32_e32 vcc, v19, v31
	v_lshl_or_b32 v33, v34, 4, v63
	ds_write_b32 v33, v42
	v_cndmask_b32_e32 v31, v31, v19, vcc
	v_cndmask_b32_e32 v30, v30, v138, vcc
	v_cmp_gt_f32_e32 vcc, v20, v31
	s_nop 1
	v_cndmask_b32_e32 v31, v31, v20, vcc
	v_cndmask_b32_e32 v30, v30, v140, vcc
	v_cmp_gt_f32_e32 vcc, v21, v31
	s_nop 1
	v_cndmask_b32_e32 v31, v31, v21, vcc
	v_cndmask_b32_e32 v30, v30, v141, vcc
	v_cmp_gt_f32_e32 vcc, v14, v31
	s_nop 1
	v_cndmask_b32_e32 v31, v31, v14, vcc
	v_cndmask_b32_e32 v30, v30, v139, vcc
	v_cmp_gt_f32_e32 vcc, v15, v31
	s_nop 1
	v_cndmask_b32_e32 v31, v31, v15, vcc
	v_cndmask_b32_e32 v30, v30, v143, vcc
	v_cmp_gt_f32_e32 vcc, v16, v31
	s_nop 1
	v_cndmask_b32_e32 v31, v31, v16, vcc
	v_cndmask_b32_e32 v30, v30, v144, vcc
	v_cmp_gt_f32_e32 vcc, v17, v31
	s_nop 1
	v_cndmask_b32_e32 v31, v31, v17, vcc
	v_max_f32_e32 v36, v31, v31
	v_cndmask_b32_e32 v30, v30, v145, vcc
	v_mov_b32_dpp v35, v31 row_ror:1 row_mask:0xf bank_mask:0xf
	v_max_f32_e32 v35, v35, v35
	v_max_f32_e32 v35, v36, v35
	v_mov_b32_e32 v36, v99
	s_nop 1
	v_mov_b32_dpp v36, v35 row_ror:2 row_mask:0xf bank_mask:0xf
	v_max_f32_e32 v36, v36, v36
	v_max_f32_e32 v35, v35, v36
	v_mov_b32_e32 v36, v99
	s_nop 1
	v_mov_b32_dpp v36, v35 row_ror:4 row_mask:0xf bank_mask:0xf
	v_max_f32_e32 v36, v36, v36
	v_max_f32_e32 v35, v35, v36
	v_mov_b32_e32 v36, v99
	s_nop 1
	v_mov_b32_dpp v36, v35 row_ror:8 row_mask:0xf bank_mask:0xf
	v_max_f32_e32 v36, v36, v36
	v_max_f32_e32 v35, v35, v36
	ds_bpermute_b32 v36, v1, v35
	s_waitcnt lgkmcnt(0)
	v_max_f32_e32 v33, v36, v36
	v_max_f32_e32 v33, v35, v33
	ds_bpermute_b32 v34, v151, v33
	v_mul_hi_u32 v35, v32, s5
	v_mad_i32_i24 v32, v35, -6, v32
	v_and_b32_e32 v42, 3, v32
	v_lshlrev_b32_e32 v135, 5, v35
	s_waitcnt lgkmcnt(0)
	v_max_f32_e32 v34, v34, v34
	v_max_f32_e32 v47, v33, v34
	v_cmp_eq_f32_e32 vcc, v31, v47
	s_ff1_i32_b64 s5, vcc
	s_cmp_lg_u64 vcc, 0
	s_cselect_b32 s5, s5, 63
	v_or_b32_e32 v31, s5, v132
	v_lshlrev_b32_e32 v31, 2, v31
	ds_bpermute_b32 v33, v31, v30
	v_lshlrev_b32_e32 v30, 2, v32
	v_and_b32_e32 v132, 0xffffff0, v30
	v_mov_b64_e32 v[30:31], s[48:49]
	v_lshlrev_b32_e32 v136, 2, v42
	s_waitcnt lgkmcnt(0)
	v_mad_i64_i32 v[30:31], s[4:5], v33, s4, v[30:31]
	v_lshl_add_u64 v[44:45], v[30:31], 0, v[98:99]
	global_load_dwordx4 v[30:33], v[44:45], off
	global_load_dwordx4 v[34:37], v[44:45], off offset:1024
	global_load_dwordx4 v[38:41], v[44:45], off offset:2048
	v_or_b32_e32 v44, v135, v150
	v_add_u32_e32 v44, v44, v132
	v_lshl_or_b32 v42, v44, 4, v136
	ds_write_b32 v42, v43
	v_or_b32_e32 v42, v100, v150
	v_lshlrev_b32_e32 v44, 4, v42
	s_waitcnt vmcnt(3)
	v_mul_f32_e32 v42, v142, v46
	s_mov_b32 s4, 0xf800000
	v_mul_f32_e32 v43, 0x4f800000, v42
	v_cmp_gt_f32_e32 vcc, s4, v42
	v_add_u32_e32 v44, 8, v44
	s_nop 0
	v_cndmask_b32_e32 v45, v42, v43, vcc
	v_sqrt_f32_e32 v46, v45
	v_mov_b64_e32 v[42:43], s[0:1]
	ds_write2st64_b64 v44, v[42:43], v[42:43] offset1:64
	v_add_u32_e32 v48, -1, v46
	v_fma_f32 v49, -v48, v46, v45
	v_cmp_ge_f32_e64 s[0:1], 0, v49
	v_add_u32_e32 v49, 1, v46
	s_nop 0
	v_cndmask_b32_e64 v48, v46, v48, s[0:1]
	v_fma_f32 v46, -v49, v46, v45
	v_cmp_lt_f32_e64 s[0:1], 0, v46
	s_nop 1
	v_cndmask_b32_e64 v46, v48, v49, s[0:1]
	v_mul_f32_e32 v48, 0x37800000, v46
	v_cndmask_b32_e32 v46, v46, v48, vcc
	v_mov_b32_e32 v48, 0x260
	v_cmp_class_f32_e32 vcc, v45, v48
	s_nop 1
	v_cndmask_b32_e32 v45, v46, v45, vcc
	v_fmamk_f32 v45, v45, 0xbbb8cfc0, v47
	v_cmp_ge_f32_e64 s[34:35], v26, v45
	v_cmp_ge_f32_e64 s[30:31], v27, v45
	s_bcnt1_i32_b64 s0, s[34:35]
	s_bcnt1_i32_b64 s1, s[30:31]
	v_cmp_ge_f32_e64 s[28:29], v28, v45
	s_add_i32 s0, s0, s1
	s_bcnt1_i32_b64 s1, s[28:29]
	v_cmp_ge_f32_e64 s[26:27], v29, v45
	s_add_i32 s0, s0, s1
	s_bcnt1_i32_b64 s1, s[26:27]
	v_cmp_ge_f32_e64 s[24:25], v22, v45
	s_add_i32 s0, s0, s1
	s_bcnt1_i32_b64 s1, s[24:25]
	v_cmp_ge_f32_e64 s[22:23], v23, v45
	s_add_i32 s0, s0, s1
	s_bcnt1_i32_b64 s1, s[22:23]
	v_cmp_ge_f32_e64 s[20:21], v24, v45
	s_add_i32 s0, s0, s1
	s_bcnt1_i32_b64 s1, s[20:21]
	v_cmp_ge_f32_e64 s[18:19], v25, v45
	s_add_i32 s0, s0, s1
	s_bcnt1_i32_b64 s1, s[18:19]
	v_cmp_ge_f32_e64 s[16:17], v18, v45
	s_add_i32 s0, s0, s1
	s_bcnt1_i32_b64 s1, s[16:17]
	v_cmp_ge_f32_e64 s[14:15], v19, v45
	s_add_i32 s0, s0, s1
	s_bcnt1_i32_b64 s1, s[14:15]
	v_cmp_ge_f32_e64 s[12:13], v20, v45
	s_add_i32 s0, s0, s1
	s_bcnt1_i32_b64 s1, s[12:13]
	v_cmp_ge_f32_e64 s[10:11], v21, v45
	s_add_i32 s0, s0, s1
	s_bcnt1_i32_b64 s1, s[10:11]
	v_cmp_ge_f32_e64 s[8:9], v14, v45
	s_add_i32 s0, s0, s1
	s_bcnt1_i32_b64 s1, s[8:9]
	v_cmp_ge_f32_e64 s[6:7], v15, v45
	s_add_i32 s0, s0, s1
	s_bcnt1_i32_b64 s1, s[6:7]
	v_cmp_ge_f32_e64 s[4:5], v16, v45
	s_add_i32 s0, s0, s1
	s_bcnt1_i32_b64 s1, s[4:5]
	s_add_i32 s36, s0, s1
	v_cmp_ge_f32_e64 s[0:1], v17, v45
	s_bcnt1_i32_b64 s37, s[0:1]
	s_add_i32 s36, s36, s37
	s_cmp_gt_u32 s36, 64
	s_cbranch_scc1 .LBB2_214
	s_cmp_lt_u32 s36, 2
	s_waitcnt vmcnt(0)
	v_mov_b64_e32 v[16:17], v[40:41]
	v_mov_b64_e32 v[14:15], v[38:39]
	v_mov_b64_e32 v[20:21], v[36:37]
	v_mov_b64_e32 v[18:19], v[34:35]
	v_mov_b64_e32 v[24:25], v[32:33]
	v_mov_b64_e32 v[22:23], v[30:31]
	s_cbranch_scc1 .LBB2_301
	v_cndmask_b32_e64 v14, 0, 1, s[34:35]
	s_mov_b32 s50, 0
	v_cmp_ne_u32_e32 vcc, 0, v14
	s_cbranch_vccz .LBB2_215
	v_mov_b32_e32 v14, 0x1c000
	v_lshl_or_b32 v14, v150, 8, v14
	s_branch .LBB2_212

.LBB2_414:
	s_movk_i32 s0, 0xc00
	v_mov_b64_e32 v[26:27], s[42:43]
	v_mul_u32_u24_e32 v28, 0xc00, v154
	v_mad_i64_i32 v[26:27], s[0:1], v62, s0, v[26:27]
	v_or_b32_e32 v28, v28, v98
	v_mov_b32_e32 v99, 0
	v_lshl_add_u64 v[26:27], v[26:27], 0, v[98:99]
	v_or_b32_e32 v29, 0x10000, v28
	global_store_dwordx4 v[26:27], v[22:25], off sc1
	ds_write_b128 v29, v[22:25]
	v_sub_f32_e32 v10, v10, v22
	v_or_b32_e32 v22, v101, v154
	v_sub_f32_e32 v11, v11, v23
	v_add_u32_e32 v23, v22, v102
	v_lshl_or_b32 v23, v23, 4, v103
	ds_write_b32 v23, v10
	v_add_u32_e32 v10, v22, v104
	v_lshl_or_b32 v10, v10, 4, v105
	ds_write_b32 v10, v11
	v_or_b32_e32 v10, v106, v154
	v_add_u32_e32 v10, v10, v107
	v_sub_f32_e32 v12, v12, v24
	v_lshl_or_b32 v10, v10, 4, v108
	ds_write_b32 v10, v12
	v_or_b32_e32 v10, v109, v154
	v_add_u32_e32 v10, v10, v110
	v_sub_f32_e32 v13, v13, v25
	v_lshl_or_b32 v10, v10, 4, v111
	ds_write_b32 v10, v13
	v_add_u32_e32 v10, 0x10400, v28
	ds_write_b128 v10, v[18:21]
	v_sub_f32_e32 v10, v6, v18
	v_sub_f32_e32 v11, v7, v19
	v_pk_add_f32 v[6:7], v[8:9], v[20:21] neg_lo:[0,1] neg_hi:[0,1]
	v_or_b32_e32 v8, v112, v154
	v_add_u32_e32 v9, v8, v113
	v_add_u32_e32 v8, v8, v115
	v_lshl_or_b32 v9, v9, 4, v114
	v_lshl_or_b32 v8, v8, 4, v116
	ds_write_b32 v9, v10
	ds_write_b32 v8, v11
	v_or_b32_e32 v8, v117, v154
	v_add_u32_e32 v8, v8, v118
	v_lshl_or_b32 v8, v8, 4, v119
	ds_write_b32 v8, v6
	v_or_b32_e32 v6, v120, v154
	v_add_u32_e32 v6, v6, v121
	v_lshl_or_b32 v6, v6, 4, v122
	ds_write_b32 v6, v7
	v_add_u32_e32 v6, 0x10800, v28
	ds_write_b128 v6, v[14:17]
	v_or_b32_e32 v6, v123, v154
	v_add_u32_e32 v7, v6, v124
	v_pk_add_f32 v[2:3], v[2:3], v[14:15] neg_lo:[0,1] neg_hi:[0,1]
	v_lshl_or_b32 v7, v7, 4, v125
	ds_write_b32 v7, v2
	v_add_u32_e32 v2, v6, v126
	v_lshl_or_b32 v2, v2, 4, v127
	ds_write_b32 v2, v3
	v_or_b32_e32 v2, v133, v154
	v_add_u32_e32 v2, v2, v134
	v_pk_add_f32 v[4:5], v[4:5], v[16:17] neg_lo:[0,1] neg_hi:[0,1]
	v_lshl_or_b32 v2, v2, 4, v63
	ds_write_b32 v2, v4
	v_or_b32_e32 v2, v135, v154
	v_add_u32_e32 v2, v2, v132
	v_lshl_or_b32 v2, v2, 4, v136
	v_add_lshl_u32 v4, v100, v154, 4
	s_mov_b32 s5, 0
	s_mov_b32 s4, 1.0
	ds_write_b32 v2, v5
	v_mov_b64_e32 v[2:3], s[4:5]
	v_add_u32_e32 v4, 8, v4
	s_waitcnt vmcnt(1)
	v_lshlrev_b32_e32 v40, 9, v150
	ds_write2st64_b64 v4, v[2:3], v[2:3] offset1:64
	v_or_b32_e32 v2, v40, v128
	v_lshlrev_b32_e32 v98, 4, v2
	v_lshl_add_u64 v[100:101], s[40:41], 0, v[98:99]
	s_mov_b64 s[0:1], 0x787000
	v_lshl_add_u64 v[34:35], v[100:101], 0, s[0:1]
	s_mov_b32 s0, 0x788000
	v_add_co_u32_e32 v36, vcc, s0, v100
	global_store_dwordx4 v[26:27], v[18:21], off offset:1024 sc1
	global_store_dwordx4 v[26:27], v[14:17], off offset:2048 sc1
	s_waitcnt lgkmcnt(0)
	s_barrier
	v_addc_co_u32_e32 v37, vcc, 0, v101, vcc
	s_lshr_b32 s59, s33, 4
	s_and_b32 s59, s59, 31
	s_lshl_b32 s59, s59, 15
	s_add_u32 s59, s59, 0x787000
	s_add_u32 s68, s40, s59
	s_addc_u32 s69, s41, 0
	v_lshlrev_b32_e32 v207, 6, v0
	global_load_dword v207, v207, s[68:69]
	global_load_dwordx4 v[2:5], v[34:35], off offset:1024
	global_load_dwordx4 v[10:13], v[34:35], off offset:2048
	global_load_dwordx4 v[14:17], v[34:35], off offset:3072
	global_load_dwordx4 v[6:9], v[36:37], off offset:-4096
	global_load_dwordx4 v[18:21], v[36:37], off
	global_load_dwordx4 v[22:25], v[36:37], off offset:1024
	global_load_dwordx4 v[26:29], v[36:37], off offset:2048
	global_load_dwordx4 v[30:33], v[36:37], off offset:3072
	v_and_b32_e32 v35, 15, v0
	v_lshrrev_b32_e32 v37, 4, v128
	v_lshlrev_b32_e32 v102, 2, v35
	v_lshlrev_b32_e32 v41, 2, v37
	v_lshlrev_b32_e32 v34, 4, v35
	v_cmp_gt_u32_e64 s[0:1], 6, v35
	v_mov_b32_e32 v35, v99
	v_or3_b32 v36, v34, v41, v40
	v_lshl_add_u64 v[104:105], s[44:45], 0, v[34:35]
	v_or_b32_e32 v34, v40, v34
	s_movk_i32 s4, 0x1000
	v_or3_b32 v153, v34, v41, s4
	v_or_b32_e32 v34, 0x11800, v98
	v_lshl_add_u64 v[118:119], s[40:41], 0, v[34:35]
	v_or_b32_e32 v34, 0x11400, v98
	v_lshl_add_u64 v[120:121], s[40:41], 0, v[34:35]
	v_or_b32_e32 v34, 0x11000, v98
	ds_read2st64_b32 v[132:133], v36 offset1:1
	v_or_b32_e32 v36, s33, v41
	v_lshl_add_u64 v[122:123], s[40:41], 0, v[34:35]
	v_or_b32_e32 v34, 0x10c00, v98
	v_or_b32_e32 v38, 1, v36
	v_lshl_add_u64 v[124:125], s[40:41], 0, v[34:35]
	v_or_b32_e32 v34, 0x10800, v98
	v_mul_u32_u24_e32 v152, 0x3000, v37
	v_ashrrev_i32_e32 v37, 31, v36
	v_ashrrev_i32_e32 v39, 31, v38
	v_lshl_add_u64 v[126:127], s[40:41], 0, v[34:35]
	v_or_b32_e32 v34, 0x10400, v98
	v_mov_b32_e32 v103, v99
	v_lshlrev_b64 v[108:109], 17, v[36:37]
	v_lshlrev_b64 v[110:111], 17, v[38:39]
	v_or_b32_e32 v38, 2, v36
	v_or_b32_e32 v36, 3, v36
	v_lshl_add_u64 v[128:129], s[40:41], 0, v[34:35]
	v_mul_u32_u24_e32 v34, 24, v150
	v_lshl_add_u64 v[106:107], s[38:39], 0, v[102:103]
	v_ashrrev_i32_e32 v39, 31, v38
	v_ashrrev_i32_e32 v37, 31, v36
	v_lshlrev_b32_e32 v103, 2, v0
	v_or_b32_e32 v98, 0x11c00, v98
	v_or_b32_e32 v34, v152, v34
	v_lshlrev_b64 v[112:113], 17, v[38:39]
	v_lshlrev_b64 v[114:115], 17, v[36:37]
	v_and_b32_e32 v116, 0x700, v103
	v_mov_b32_e32 v117, v99
	v_lshl_add_u64 v[130:131], s[40:41], 0, v[98:99]
	v_add_u32_e32 v154, v34, v102
	s_mov_b64 s[6:7], 0
	s_mov_b64 s[8:9], 0x800
	v_mov_b32_e32 v155, 0x400
	v_mov_b32_e32 v159, 0
	v_mov_b32_e32 v158, 0
	v_mov_b32_e32 v157, 0
	v_mov_b32_e32 v156, 0
	v_readfirstlane_b32 s78, v150
	v_and_b32_e32 v104, 63, v0
	v_lshlrev_b32_e32 v104, 4, v104
	v_lshl_or_b32 v104, v150, 13, v104
	v_add_u32_e32 v105, 0xfffff000, v153
	v_mov_b32_e32 v106, v154
	v_lshrrev_b32_e32 v98, 2, v102
	v_cmp_gt_u32_e32 vcc, 6, v98
	v_add_u32_e32 v107, -6, v98
	s_nop 0
	v_cndmask_b32_e32 v107, v107, v98, vcc
	v_cmp_gt_u32_e32 vcc, 6, v107
	v_add_u32_e32 v98, -6, v107
	s_nop 0
	v_cndmask_b32_e32 v107, v98, v107, vcc
	v_lshlrev_b32_e32 v107, 2, v107
	v_sub_u32_e32 v106, v106, v102
	v_add_u32_e32 v106, v106, v107
	v_and_b32_e32 v98, 63, v0
	v_lshrrev_b32_e32 v98, 4, v98
	v_lshlrev_b32_e32 v98, 19, v98
	v_lshl_or_b32 v108, v102, 2, v98
	v_add_u32_e32 v109, 0x20000, v108
	v_add_u32_e32 v110, 0x40000, v108
	v_add_u32_e32 v111, 0x60000, v108
	v_mov_b32_e32 v240, 0
	v_mov_b32_e32 v241, 0
	v_mov_b32_e32 v242, 0
	v_mov_b32_e32 v243, 0
	s_lshl_b32 s84, s33, 17
	s_lshl_b32 s85, s78, 10
	s_add_u32 s84, s84, s85
	s_add_u32 s80, s44, s84
	s_addc_u32 s81, s45, 0
	s_mul_i32 s84, s78, 0x1800
	s_add_u32 s94, s38, s84
	s_addc_u32 s95, s39, 0
	s_mov_b32 s70, 0
	s_add_u32 s86, s40, 0x797000
	s_addc_u32 s87, s41, 0
	s_add_u32 s88, s86, 0x1000
	s_addc_u32 s89, s87, 0
	v_add_u32_e32 v112, 0x1000, v105
	s_waitcnt vmcnt(0) lgkmcnt(0)
	v_mfma_f32_16x16x4_f32 v[34:37], v132, v6, 0
	v_mfma_f32_16x16x4_f32 v[38:41], v132, v8, 0
	v_mfma_f32_16x16x4_f32 v[34:37], v133, v7, v[34:37]
	v_mfma_f32_16x16x4_f32 v[38:41], v133, v9, v[38:41]
	global_load_dwordx4 v[6:9], v104, s[86:87]
	v_mfma_f32_16x16x4_f32 v[42:45], v132, v2, 0
	v_mfma_f32_16x16x4_f32 v[46:49], v132, v4, 0
	v_mfma_f32_16x16x4_f32 v[42:45], v133, v3, v[42:45]
	v_mfma_f32_16x16x4_f32 v[46:49], v133, v5, v[46:49]
	global_load_dwordx4 v[2:5], v104, s[86:87] offset:1024
	v_mfma_f32_16x16x4_f32 v[50:53], v132, v10, 0
	v_mfma_f32_16x16x4_f32 v[54:57], v132, v12, 0
	v_mfma_f32_16x16x4_f32 v[50:53], v133, v11, v[50:53]
	v_mfma_f32_16x16x4_f32 v[54:57], v133, v13, v[54:57]
	global_load_dwordx4 v[10:13], v104, s[86:87] offset:2048
	v_mfma_f32_16x16x4_f32 v[58:61], v132, v14, 0
	v_mfma_f32_16x16x4_f32 v[62:65], v132, v16, 0
	v_mfma_f32_16x16x4_f32 v[58:61], v133, v15, v[58:61]
	v_mfma_f32_16x16x4_f32 v[62:65], v133, v17, v[62:65]
	global_load_dwordx4 v[14:17], v104, s[86:87] offset:3072
	v_mfma_f32_16x16x4_f32 v[66:69], v132, v18, 0
	v_mfma_f32_16x16x4_f32 v[70:73], v132, v20, 0
	v_mfma_f32_16x16x4_f32 v[66:69], v133, v19, v[66:69]
	v_mfma_f32_16x16x4_f32 v[70:73], v133, v21, v[70:73]
	global_load_dwordx4 v[18:21], v104, s[88:89]
	v_mfma_f32_16x16x4_f32 v[74:77], v132, v22, 0
	v_mfma_f32_16x16x4_f32 v[78:81], v132, v24, 0
	v_mfma_f32_16x16x4_f32 v[74:77], v133, v23, v[74:77]
	v_mfma_f32_16x16x4_f32 v[78:81], v133, v25, v[78:81]
	global_load_dwordx4 v[22:25], v104, s[88:89] offset:1024
	v_mfma_f32_16x16x4_f32 v[82:85], v132, v26, 0
	v_mfma_f32_16x16x4_f32 v[86:89], v132, v28, 0
	v_mfma_f32_16x16x4_f32 v[82:85], v133, v27, v[82:85]
	v_mfma_f32_16x16x4_f32 v[86:89], v133, v29, v[86:89]
	global_load_dwordx4 v[26:29], v104, s[88:89] offset:2048
	v_mfma_f32_16x16x4_f32 v[90:93], v132, v30, 0
	v_mfma_f32_16x16x4_f32 v[94:97], v132, v32, 0
	v_mfma_f32_16x16x4_f32 v[90:93], v133, v31, v[90:93]
	v_mfma_f32_16x16x4_f32 v[94:97], v133, v33, v[94:97]
	global_load_dwordx4 v[30:33], v104, s[88:89] offset:3072
	ds_read2st64_b32 v[132:133], v112 offset1:1
	s_nop 7
	s_nop 7
	v_max3_f32 v114, v34, v38, v42
	v_max3_f32 v116, v46, v50, v54
	v_max3_f32 v114, v114, v58, v62
	v_max3_f32 v116, v116, v66, v70
	v_max3_f32 v114, v114, v74, v78
	v_max3_f32 v116, v116, v82, v86
	v_max3_f32 v114, v114, v90, v94
	v_max_f32_e32 v114, v114, v116
	s_nop 1
	v_max_f32_dpp v114, v114, v114 row_ror:1 row_mask:0xf bank_mask:0xf
	s_nop 1
	v_max_f32_dpp v114, v114, v114 row_ror:2 row_mask:0xf bank_mask:0xf
	s_nop 1
	v_max_f32_dpp v114, v114, v114 row_ror:4 row_mask:0xf bank_mask:0xf
	s_nop 1
	v_max_f32_dpp v114, v114, v114 row_ror:8 row_mask:0xf bank_mask:0xf
	s_waitcnt vmcnt(0) lgkmcnt(0)

.LBB2_525:
	v_mov_b32_e32 v1, 0x1ca00
	ds_read_b128 v[36:39], v1
	v_mov_b32_e32 v2, 0x1ca10
	ds_read_b128 v[40:43], v2
	v_mov_b32_e32 v1, 0
	v_lshl_add_u64 v[2:3], s[46:47], 0, v[0:1]
	s_waitcnt lgkmcnt(1)
	v_div_scale_f32 v44, s[4:5], v36, v36, v35
	v_rcp_f32_e32 v45, v44
	v_div_scale_f32 v1, vcc, v35, v36, v35
	s_or_b32 s6, s33, 1
	v_fma_f32 v46, -v44, v45, 1.0
	v_fmac_f32_e32 v45, v46, v45
	v_mul_f32_e32 v46, v1, v45
	v_fma_f32 v47, -v44, v46, v1
	v_fmac_f32_e32 v46, v47, v45
	v_fma_f32 v1, -v44, v46, v1
	v_div_fmas_f32 v1, v1, v45, v46
	v_div_fixup_f32 v1, v1, v36, v35
	v_div_scale_f32 v35, s[4:5], v37, v37, v32
	v_rcp_f32_e32 v36, v35
	v_mov_b32_e32 v46, 0xc00
	v_mad_i64_i32 v[44:45], s[4:5], s33, v46, v[2:3]
	global_store_dword v[44:45], v1, off sc1
	v_fma_f32 v1, -v35, v36, 1.0
	v_fmac_f32_e32 v36, v1, v36
	v_div_scale_f32 v1, vcc, v32, v37, v32
	v_mul_f32_e32 v44, v1, v36
	v_fma_f32 v45, -v35, v44, v1
	v_fmac_f32_e32 v44, v45, v36
	v_fma_f32 v1, -v35, v44, v1
	v_div_fmas_f32 v1, v1, v36, v44
	v_div_fixup_f32 v1, v1, v37, v32
	v_div_scale_f32 v32, s[4:5], v38, v38, v34
	v_rcp_f32_e32 v35, v32
	v_mad_i64_i32 v[36:37], s[4:5], s6, v46, v[2:3]
	global_store_dword v[36:37], v1, off sc1
	v_fma_f32 v1, -v32, v35, 1.0
	v_fmac_f32_e32 v35, v1, v35
	v_div_scale_f32 v1, vcc, v34, v38, v34
	v_mul_f32_e32 v36, v1, v35
	v_fma_f32 v37, -v32, v36, v1
	v_fmac_f32_e32 v36, v37, v35
	v_fma_f32 v1, -v32, v36, v1
	v_div_scale_f32 v32, s[4:5], v39, v39, v31
	v_div_fmas_f32 v1, v1, v35, v36
	v_rcp_f32_e32 v36, v32
	s_or_b32 s6, s33, 2
	v_div_fixup_f32 v1, v1, v38, v34
	v_mad_i64_i32 v[34:35], s[4:5], s6, v46, v[2:3]
	global_store_dword v[34:35], v1, off sc1
	v_fma_f32 v1, -v32, v36, 1.0
	v_fmac_f32_e32 v36, v1, v36
	v_div_scale_f32 v1, vcc, v31, v39, v31
	v_mul_f32_e32 v34, v1, v36
	v_fma_f32 v35, -v32, v34, v1
	v_fmac_f32_e32 v34, v35, v36
	v_fma_f32 v1, -v32, v34, v1
	v_div_fmas_f32 v1, v1, v36, v34
	v_div_fixup_f32 v1, v1, v39, v31
	s_waitcnt lgkmcnt(0)
	v_div_scale_f32 v31, s[4:5], v40, v40, v33
	v_rcp_f32_e32 v32, v31
	s_or_b32 s6, s33, 3
	v_mad_i64_i32 v[34:35], s[4:5], s6, v46, v[2:3]
	global_store_dword v[34:35], v1, off sc1
	v_fma_f32 v1, -v31, v32, 1.0
	v_fmac_f32_e32 v32, v1, v32
	v_div_scale_f32 v1, vcc, v33, v40, v33
	v_mul_f32_e32 v34, v1, v32
	v_fma_f32 v35, -v31, v34, v1
	v_fmac_f32_e32 v34, v35, v32
	v_fma_f32 v1, -v31, v34, v1
	v_div_scale_f32 v31, s[4:5], v41, v41, v29
	v_div_fmas_f32 v1, v1, v32, v34
	v_rcp_f32_e32 v34, v31
	s_or_b32 s6, s33, 4
	v_div_fixup_f32 v1, v1, v40, v33
	v_mad_i64_i32 v[32:33], s[4:5], s6, v46, v[2:3]
	global_store_dword v[32:33], v1, off sc1
	v_fma_f32 v1, -v31, v34, 1.0
	v_fmac_f32_e32 v34, v1, v34
	v_div_scale_f32 v1, vcc, v29, v41, v29
	v_mul_f32_e32 v32, v1, v34
	v_fma_f32 v33, -v31, v32, v1
	v_fmac_f32_e32 v32, v33, v34
	v_fma_f32 v1, -v31, v32, v1
	v_div_fmas_f32 v1, v1, v34, v32
	v_div_fixup_f32 v1, v1, v41, v29
	v_div_scale_f32 v29, s[4:5], v42, v42, v30
	v_rcp_f32_e32 v31, v29
	s_or_b32 s6, s33, 5
	v_mad_i64_i32 v[32:33], s[4:5], s6, v46, v[2:3]
	global_store_dword v[32:33], v1, off sc1
	v_fma_f32 v1, -v29, v31, 1.0
	v_fmac_f32_e32 v31, v1, v31
	v_div_scale_f32 v1, vcc, v30, v42, v30
	v_mul_f32_e32 v32, v1, v31
	v_fma_f32 v33, -v29, v32, v1
	v_fmac_f32_e32 v32, v33, v31
	v_fma_f32 v1, -v29, v32, v1
	v_div_scale_f32 v29, s[4:5], v43, v43, v28
	v_div_fmas_f32 v1, v1, v31, v32
	v_rcp_f32_e32 v32, v29
	s_or_b32 s6, s33, 6
	v_div_fixup_f32 v1, v1, v42, v30
	v_mad_i64_i32 v[30:31], s[4:5], s6, v46, v[2:3]
	global_store_dword v[30:31], v1, off sc1
	v_fma_f32 v1, -v29, v32, 1.0
	v_fmac_f32_e32 v32, v1, v32
	v_div_scale_f32 v1, vcc, v28, v43, v28
	v_mul_f32_e32 v30, v1, v32
	v_fma_f32 v31, -v29, v30, v1
	v_fmac_f32_e32 v30, v31, v32
	v_fma_f32 v1, -v29, v30, v1
	v_div_fmas_f32 v1, v1, v32, v30
	v_div_fixup_f32 v1, v1, v43, v28
	v_mov_b32_e32 v28, 0x1ca20
	ds_read_b128 v[28:31], v28
	v_mov_b32_e32 v32, 0x1ca30
	ds_read_b128 v[32:35], v32
	s_or_b32 s6, s33, 7
	v_mad_i64_i32 v[36:37], s[4:5], s6, v46, v[2:3]
	s_waitcnt lgkmcnt(1)
	v_div_scale_f32 v38, s[4:5], v28, v28, v27
	v_rcp_f32_e32 v39, v38
	global_store_dword v[36:37], v1, off sc1
	s_or_b32 s6, s33, 8
	v_fma_f32 v1, -v38, v39, 1.0
	v_fmac_f32_e32 v39, v1, v39
	v_div_scale_f32 v1, vcc, v27, v28, v27
	v_mul_f32_e32 v36, v1, v39
	v_fma_f32 v37, -v38, v36, v1
	v_fmac_f32_e32 v36, v37, v39
	v_fma_f32 v1, -v38, v36, v1
	v_div_fmas_f32 v1, v1, v39, v36
	v_div_fixup_f32 v1, v1, v28, v27
	v_div_scale_f32 v27, s[4:5], v29, v29, v24
	v_rcp_f32_e32 v28, v27
	v_mad_i64_i32 v[36:37], s[4:5], s6, v46, v[2:3]
	global_store_dword v[36:37], v1, off sc1
	v_fma_f32 v1, -v27, v28, 1.0
	v_fmac_f32_e32 v28, v1, v28
	v_div_scale_f32 v1, vcc, v24, v29, v24
	v_mul_f32_e32 v36, v1, v28
	v_fma_f32 v37, -v27, v36, v1
	v_fmac_f32_e32 v36, v37, v28
	v_fma_f32 v1, -v27, v36, v1
	v_div_fmas_f32 v1, v1, v28, v36
	v_div_fixup_f32 v1, v1, v29, v24
	v_div_scale_f32 v24, s[4:5], v30, v30, v26
	v_rcp_f32_e32 v27, v24
	s_or_b32 s6, s33, 9
	v_mad_i64_i32 v[28:29], s[4:5], s6, v46, v[2:3]
	global_store_dword v[28:29], v1, off sc1
	v_fma_f32 v1, -v24, v27, 1.0
	v_fmac_f32_e32 v27, v1, v27
	v_div_scale_f32 v1, vcc, v26, v30, v26
	v_mul_f32_e32 v28, v1, v27
	v_fma_f32 v29, -v24, v28, v1
	v_fmac_f32_e32 v28, v29, v27
	v_fma_f32 v1, -v24, v28, v1
	v_div_scale_f32 v24, s[4:5], v31, v31, v23
	v_div_fmas_f32 v1, v1, v27, v28
	v_rcp_f32_e32 v28, v24
	s_or_b32 s6, s33, 10
	v_div_fixup_f32 v1, v1, v30, v26
	v_mad_i64_i32 v[26:27], s[4:5], s6, v46, v[2:3]
	global_store_dword v[26:27], v1, off sc1
	v_fma_f32 v1, -v24, v28, 1.0
	v_fmac_f32_e32 v28, v1, v28
	v_div_scale_f32 v1, vcc, v23, v31, v23
	v_mul_f32_e32 v26, v1, v28
	v_fma_f32 v27, -v24, v26, v1
	v_fmac_f32_e32 v26, v27, v28
	v_fma_f32 v1, -v24, v26, v1
	v_div_fmas_f32 v1, v1, v28, v26
	v_div_fixup_f32 v1, v1, v31, v23
	s_waitcnt lgkmcnt(0)
	v_div_scale_f32 v23, s[4:5], v32, v32, v25
	v_rcp_f32_e32 v24, v23
	s_or_b32 s6, s33, 11
	v_mad_i64_i32 v[26:27], s[4:5], s6, v46, v[2:3]
	global_store_dword v[26:27], v1, off sc1
	v_fma_f32 v1, -v23, v24, 1.0
	v_fmac_f32_e32 v24, v1, v24
	v_div_scale_f32 v1, vcc, v25, v32, v25
	v_mul_f32_e32 v26, v1, v24
	v_fma_f32 v27, -v23, v26, v1
	v_fmac_f32_e32 v26, v27, v24
	v_fma_f32 v1, -v23, v26, v1
	v_div_scale_f32 v23, s[4:5], v33, v33, v21
	v_div_fmas_f32 v1, v1, v24, v26
	v_rcp_f32_e32 v26, v23
	s_or_b32 s6, s33, 12
	v_div_fixup_f32 v1, v1, v32, v25
	v_mad_i64_i32 v[24:25], s[4:5], s6, v46, v[2:3]
	global_store_dword v[24:25], v1, off sc1
	v_fma_f32 v1, -v23, v26, 1.0
	v_fmac_f32_e32 v26, v1, v26
	v_div_scale_f32 v1, vcc, v21, v33, v21
	v_mul_f32_e32 v24, v1, v26
	v_fma_f32 v25, -v23, v24, v1
	v_fmac_f32_e32 v24, v25, v26
	v_fma_f32 v1, -v23, v24, v1
	v_div_fmas_f32 v1, v1, v26, v24
	v_div_fixup_f32 v1, v1, v33, v21
	v_div_scale_f32 v21, s[4:5], v34, v34, v22
	v_rcp_f32_e32 v23, v21
	s_or_b32 s6, s33, 13
	v_mad_i64_i32 v[24:25], s[4:5], s6, v46, v[2:3]
	global_store_dword v[24:25], v1, off sc1
	v_fma_f32 v1, -v21, v23, 1.0
	v_fmac_f32_e32 v23, v1, v23
	v_div_scale_f32 v1, vcc, v22, v34, v22
	v_mul_f32_e32 v24, v1, v23
	v_fma_f32 v25, -v21, v24, v1
	v_fmac_f32_e32 v24, v25, v23
	v_fma_f32 v1, -v21, v24, v1
	v_div_scale_f32 v21, s[4:5], v35, v35, v20
	v_div_fmas_f32 v1, v1, v23, v24
	v_rcp_f32_e32 v24, v21
	s_or_b32 s6, s33, 14
	v_div_fixup_f32 v1, v1, v34, v22
	v_mad_i64_i32 v[22:23], s[4:5], s6, v46, v[2:3]
	global_store_dword v[22:23], v1, off sc1
	v_fma_f32 v1, -v21, v24, 1.0
	v_fmac_f32_e32 v24, v1, v24
	v_div_scale_f32 v1, vcc, v20, v35, v20
	v_mul_f32_e32 v22, v1, v24
	v_fma_f32 v23, -v21, v22, v1
	v_fmac_f32_e32 v22, v23, v24
	v_fma_f32 v1, -v21, v22, v1
	v_div_fmas_f32 v1, v1, v24, v22
	s_or_b32 s4, s33, 15
	v_div_fixup_f32 v1, v1, v35, v20
	v_mad_i64_i32 v[2:3], s[4:5], s4, v46, v[2:3]
	global_store_dword v[2:3], v1, off sc1
	s_or_b64 exec, exec, s[2:3]
	s_and_saveexec_b64 s[2:3], s[0:1]
	s_cbranch_execz .LBB2_524
.LBB2_526:
	v_mov_b32_e32 v1, 0x1ca00
	ds_read_b128 v[20:23], v1
	v_mov_b32_e32 v2, 0x1ca10
	ds_read_b128 v[24:27], v2
	v_mov_b32_e32 v1, 0
	v_lshl_add_u64 v[0:1], s[46:47], 0, v[0:1]
	s_waitcnt lgkmcnt(1)
	v_div_scale_f32 v2, s[0:1], v20, v20, v19
	v_rcp_f32_e32 v3, v2
	v_div_scale_f32 v28, vcc, v19, v20, v19
	s_or_b32 s2, s33, 1
	v_fma_f32 v29, -v2, v3, 1.0
	v_fmac_f32_e32 v3, v29, v3
	v_mul_f32_e32 v29, v28, v3
	v_fma_f32 v30, -v2, v29, v28
	v_fmac_f32_e32 v29, v30, v3
	v_fma_f32 v2, -v2, v29, v28
	v_div_scale_f32 v28, s[0:1], v21, v21, v16
	v_div_fmas_f32 v2, v2, v3, v29
	v_rcp_f32_e32 v29, v28
	v_div_fixup_f32 v19, v2, v20, v19
	v_mov_b32_e32 v20, 0xc00
	v_mad_i64_i32 v[2:3], s[0:1], s33, v20, v[0:1]
	global_store_dword v[2:3], v19, off offset:2048 sc1
	v_fma_f32 v2, -v28, v29, 1.0
	v_fmac_f32_e32 v29, v2, v29
	v_div_scale_f32 v2, vcc, v16, v21, v16
	v_mul_f32_e32 v3, v2, v29
	v_fma_f32 v19, -v28, v3, v2
	v_fmac_f32_e32 v3, v19, v29
	v_fma_f32 v2, -v28, v3, v2
	v_div_fmas_f32 v2, v2, v29, v3
	v_div_scale_f32 v19, s[0:1], v22, v22, v18
	v_div_fixup_f32 v16, v2, v21, v16
	v_rcp_f32_e32 v21, v19
	v_mad_i64_i32 v[2:3], s[0:1], s2, v20, v[0:1]
	global_store_dword v[2:3], v16, off offset:2048 sc1
	v_fma_f32 v2, -v19, v21, 1.0
	v_fmac_f32_e32 v21, v2, v21
	v_div_scale_f32 v2, vcc, v18, v22, v18
	v_mul_f32_e32 v3, v2, v21
	v_fma_f32 v16, -v19, v3, v2
	v_fmac_f32_e32 v3, v16, v21
	v_fma_f32 v2, -v19, v3, v2
	v_div_fmas_f32 v2, v2, v21, v3
	v_div_fixup_f32 v16, v2, v22, v18
	v_div_scale_f32 v18, s[0:1], v23, v23, v15
	v_rcp_f32_e32 v19, v18
	s_or_b32 s2, s33, 2
	v_mad_i64_i32 v[2:3], s[0:1], s2, v20, v[0:1]
	global_store_dword v[2:3], v16, off offset:2048 sc1
	v_fma_f32 v2, -v18, v19, 1.0
	v_fmac_f32_e32 v19, v2, v19
	v_div_scale_f32 v2, vcc, v15, v23, v15
	v_mul_f32_e32 v3, v2, v19
	v_fma_f32 v16, -v18, v3, v2
	v_fmac_f32_e32 v3, v16, v19
	s_waitcnt lgkmcnt(0)
	v_div_scale_f32 v16, s[0:1], v24, v24, v17
	v_fma_f32 v2, -v18, v3, v2
	v_rcp_f32_e32 v18, v16
	v_div_fmas_f32 v2, v2, v19, v3
	s_or_b32 s2, s33, 3
	v_div_fixup_f32 v15, v2, v23, v15
	v_mad_i64_i32 v[2:3], s[0:1], s2, v20, v[0:1]
	global_store_dword v[2:3], v15, off offset:2048 sc1
	v_fma_f32 v2, -v16, v18, 1.0
	v_fmac_f32_e32 v18, v2, v18
	v_div_scale_f32 v2, vcc, v17, v24, v17
	v_mul_f32_e32 v3, v2, v18
	v_fma_f32 v15, -v16, v3, v2
	v_fmac_f32_e32 v3, v15, v18
	v_fma_f32 v2, -v16, v3, v2
	v_div_fmas_f32 v2, v2, v18, v3
	v_div_scale_f32 v16, s[0:1], v25, v25, v13
	v_div_fixup_f32 v15, v2, v24, v17
	v_rcp_f32_e32 v17, v16
	s_or_b32 s2, s33, 4
	v_mad_i64_i32 v[2:3], s[0:1], s2, v20, v[0:1]
	global_store_dword v[2:3], v15, off offset:2048 sc1
	v_fma_f32 v2, -v16, v17, 1.0
	v_fmac_f32_e32 v17, v2, v17
	v_div_scale_f32 v2, vcc, v13, v25, v13
	v_mul_f32_e32 v3, v2, v17
	v_fma_f32 v15, -v16, v3, v2
	v_fmac_f32_e32 v3, v15, v17
	v_div_scale_f32 v15, s[0:1], v26, v26, v14
	v_fma_f32 v2, -v16, v3, v2
	v_rcp_f32_e32 v16, v15
	v_div_fmas_f32 v2, v2, v17, v3
	s_or_b32 s2, s33, 5
	v_div_fixup_f32 v13, v2, v25, v13
	v_mad_i64_i32 v[2:3], s[0:1], s2, v20, v[0:1]
	global_store_dword v[2:3], v13, off offset:2048 sc1
	v_fma_f32 v2, -v15, v16, 1.0
	v_fmac_f32_e32 v16, v2, v16
	v_div_scale_f32 v2, vcc, v14, v26, v14
	v_mul_f32_e32 v3, v2, v16
	v_fma_f32 v13, -v15, v3, v2
	v_fmac_f32_e32 v3, v13, v16
	v_fma_f32 v2, -v15, v3, v2
	v_div_fmas_f32 v2, v2, v16, v3
	v_div_fixup_f32 v13, v2, v26, v14
	v_div_scale_f32 v14, s[0:1], v27, v27, v12
	v_rcp_f32_e32 v15, v14
	s_or_b32 s2, s33, 6
	v_mad_i64_i32 v[2:3], s[0:1], s2, v20, v[0:1]
	global_store_dword v[2:3], v13, off offset:2048 sc1
	v_fma_f32 v2, -v14, v15, 1.0
	v_fmac_f32_e32 v15, v2, v15
	v_div_scale_f32 v2, vcc, v12, v27, v12
	v_mul_f32_e32 v3, v2, v15
	v_fma_f32 v13, -v14, v3, v2
	v_fmac_f32_e32 v3, v13, v15
	v_fma_f32 v2, -v14, v3, v2
	v_div_fmas_f32 v2, v2, v15, v3
	v_div_fixup_f32 v21, v2, v27, v12
	v_mov_b32_e32 v2, 0x1ca20
	ds_read_b128 v[12:15], v2
	s_or_b32 s2, s33, 7
	v_mov_b32_e32 v2, 0x1ca30
	ds_read_b128 v[16:19], v2
	v_mad_i64_i32 v[2:3], s[0:1], s2, v20, v[0:1]
	s_waitcnt lgkmcnt(1)
	v_div_scale_f32 v22, s[0:1], v12, v12, v11
	v_rcp_f32_e32 v23, v22
	global_store_dword v[2:3], v21, off offset:2048 sc1
	s_or_b32 s2, s33, 8
	v_fma_f32 v2, -v22, v23, 1.0
	v_fmac_f32_e32 v23, v2, v23
	v_div_scale_f32 v2, vcc, v11, v12, v11
	v_mul_f32_e32 v3, v2, v23
	v_fma_f32 v21, -v22, v3, v2
	v_fmac_f32_e32 v3, v21, v23
	v_fma_f32 v2, -v22, v3, v2
	v_div_fmas_f32 v2, v2, v23, v3
	v_div_fixup_f32 v11, v2, v12, v11
	v_div_scale_f32 v12, s[0:1], v13, v13, v8
	v_rcp_f32_e32 v21, v12
	v_mad_i64_i32 v[2:3], s[0:1], s2, v20, v[0:1]
	global_store_dword v[2:3], v11, off offset:2048 sc1
	v_fma_f32 v2, -v12, v21, 1.0
	v_fmac_f32_e32 v21, v2, v21
	v_div_scale_f32 v2, vcc, v8, v13, v8
	v_mul_f32_e32 v3, v2, v21
	v_fma_f32 v11, -v12, v3, v2
	v_fmac_f32_e32 v3, v11, v21
	v_div_scale_f32 v11, s[0:1], v14, v14, v10
	v_fma_f32 v2, -v12, v3, v2
	v_rcp_f32_e32 v12, v11
	v_div_fmas_f32 v2, v2, v21, v3
	s_or_b32 s2, s33, 9
	v_div_fixup_f32 v8, v2, v13, v8
	v_mad_i64_i32 v[2:3], s[0:1], s2, v20, v[0:1]
	global_store_dword v[2:3], v8, off offset:2048 sc1
	v_fma_f32 v2, -v11, v12, 1.0
	v_fmac_f32_e32 v12, v2, v12
	v_div_scale_f32 v2, vcc, v10, v14, v10
	v_mul_f32_e32 v3, v2, v12
	v_fma_f32 v8, -v11, v3, v2
	v_fmac_f32_e32 v3, v8, v12
	v_fma_f32 v2, -v11, v3, v2
	v_div_fmas_f32 v2, v2, v12, v3
	v_div_fixup_f32 v8, v2, v14, v10
	v_div_scale_f32 v10, s[0:1], v15, v15, v7
	v_rcp_f32_e32 v11, v10
	s_or_b32 s2, s33, 10
	v_mad_i64_i32 v[2:3], s[0:1], s2, v20, v[0:1]
	global_store_dword v[2:3], v8, off offset:2048 sc1
	v_fma_f32 v2, -v10, v11, 1.0
	v_fmac_f32_e32 v11, v2, v11
	v_div_scale_f32 v2, vcc, v7, v15, v7
	v_mul_f32_e32 v3, v2, v11
	v_fma_f32 v8, -v10, v3, v2
	v_fmac_f32_e32 v3, v8, v11
	s_waitcnt lgkmcnt(0)
	v_div_scale_f32 v8, s[0:1], v16, v16, v9
	v_fma_f32 v2, -v10, v3, v2
	v_rcp_f32_e32 v10, v8
	v_div_fmas_f32 v2, v2, v11, v3
	s_or_b32 s2, s33, 11
	v_div_fixup_f32 v7, v2, v15, v7
	v_mad_i64_i32 v[2:3], s[0:1], s2, v20, v[0:1]
	global_store_dword v[2:3], v7, off offset:2048 sc1
	v_fma_f32 v2, -v8, v10, 1.0
	v_fmac_f32_e32 v10, v2, v10
	v_div_scale_f32 v2, vcc, v9, v16, v9
	v_mul_f32_e32 v3, v2, v10
	v_fma_f32 v7, -v8, v3, v2
	v_fmac_f32_e32 v3, v7, v10
	v_fma_f32 v2, -v8, v3, v2
	v_div_fmas_f32 v2, v2, v10, v3
	v_div_scale_f32 v8, s[0:1], v17, v17, v5
	v_div_fixup_f32 v7, v2, v16, v9
	v_rcp_f32_e32 v9, v8
	s_or_b32 s2, s33, 12
	v_mad_i64_i32 v[2:3], s[0:1], s2, v20, v[0:1]
	global_store_dword v[2:3], v7, off offset:2048 sc1
	v_fma_f32 v2, -v8, v9, 1.0
	v_fmac_f32_e32 v9, v2, v9
	v_div_scale_f32 v2, vcc, v5, v17, v5
	v_mul_f32_e32 v3, v2, v9
	v_fma_f32 v7, -v8, v3, v2
	v_fmac_f32_e32 v3, v7, v9
	v_div_scale_f32 v7, s[0:1], v18, v18, v6
	v_fma_f32 v2, -v8, v3, v2
	v_rcp_f32_e32 v8, v7
	v_div_fmas_f32 v2, v2, v9, v3
	s_or_b32 s2, s33, 13
	v_div_fixup_f32 v5, v2, v17, v5
	v_mad_i64_i32 v[2:3], s[0:1], s2, v20, v[0:1]
	global_store_dword v[2:3], v5, off offset:2048 sc1
	v_fma_f32 v2, -v7, v8, 1.0
	v_fmac_f32_e32 v8, v2, v8
	v_div_scale_f32 v2, vcc, v6, v18, v6
	v_mul_f32_e32 v3, v2, v8
	v_fma_f32 v5, -v7, v3, v2
	v_fmac_f32_e32 v3, v5, v8
	v_fma_f32 v2, -v7, v3, v2
	v_div_fmas_f32 v2, v2, v8, v3
	v_div_fixup_f32 v5, v2, v18, v6
	v_div_scale_f32 v6, s[0:1], v19, v19, v4
	v_rcp_f32_e32 v7, v6
	s_or_b32 s2, s33, 14
	v_mad_i64_i32 v[2:3], s[0:1], s2, v20, v[0:1]
	global_store_dword v[2:3], v5, off offset:2048 sc1
	v_fma_f32 v2, -v6, v7, 1.0
	v_fmac_f32_e32 v7, v2, v7
	v_div_scale_f32 v2, vcc, v4, v19, v4
	v_mul_f32_e32 v3, v2, v7
	v_fma_f32 v5, -v6, v3, v2
	v_fmac_f32_e32 v3, v5, v7
	v_fma_f32 v2, -v6, v3, v2
	v_div_fmas_f32 v2, v2, v7, v3
	s_or_b32 s0, s33, 15
	v_div_fixup_f32 v2, v2, v19, v4
	v_mad_i64_i32 v[0:1], s[0:1], s0, v20, v[0:1]
	global_store_dword v[0:1], v2, off offset:2048 sc1
	s_endpgm
